# speedup vs baseline: 1.0090x; 1.0090x over previous
.LBB2_12:
	s_add_i32 s12, s29, -1
	s_and_b32 s30, s12, 1
	s_bitcmp1_b32 s12, 1
	s_cselect_b32 s4, 0x10001, 0
	v_lshl_add_u32 v47, s30, 17, v39
	s_lshl_b32 s31, s30, 14
	s_lshl_b64 s[10:11], s[12:13], 12
	v_add_u32_e32 v48, 0x1000, v47
	v_add_u32_e32 v49, 0x2000, v47
	v_add_u32_e32 v50, 0x3000, v47
	v_or_b32_e32 v110, s31, v34
	v_add_u32_e32 v111, s31, v121
	v_lshl_add_u64 v[112:113], v[24:25], 0, s[10:11]
	v_add_u32_e32 v124, s31, v122
	v_add_u32_e32 v125, s31, v123
	s_lshl_b32 s32, s29, 13
	s_add_i32 s32, s32, 0x4000
	s_min_u32 s32, s32, 0xfe000
	s_mov_b32 s33, 0
	v_lshl_add_u64 v[114:115], v[20:21], 0, s[32:33]
	v_lshl_add_u64 v[118:119], v[22:23], 0, s[32:33]
	v_add_co_u32_e32 v116, vcc, 0x1000, v114
	v_mov_b64_e32 v[62:63], 0
	v_mov_b64_e32 v[64:65], 0
	v_addc_co_u32_e32 v117, vcc, 0, v115, vcc
	v_mov_b64_e32 v[66:67], 0
	v_mov_b64_e32 v[68:69], 0
	s_mov_b32 s31, 0
	s_sleep 1

.LBB2_20:
	s_mov_b64 exec, -1
	s_waitcnt lgkmcnt(0)
	s_barrier
	ds_read_b128 v[50:53], v111
	ds_read_b128 v[54:57], v111 offset:4096
	ds_read_b128 v[58:61], v111 offset:8192
	ds_read_b128 v[70:73], v111 offset:12288
	ds_read_b128 v[78:81], v124
	ds_read_b128 v[82:85], v124 offset:4096
	ds_read_b128 v[86:89], v124 offset:8192
	ds_read_b128 v[90:93], v124 offset:12288
	ds_read_b128 v[94:97], v125
	ds_read_b128 v[98:101], v125 offset:4096
	ds_read_b128 v[102:105], v125 offset:8192
	ds_read_b128 v[106:109], v125 offset:12288
	v_smfmac_f32_16x16x64_f16 v[62:65], v[0:3], a[0:7], v28
	v_smfmac_f32_16x16x64_f16 v[66:69], v[0:3], a[128:135], v28
	v_mov_b32_e32 v29, v128
	v_mov_b32_e32 v30, v129
	v_mov_b32_e32 v31, v130
	v_mov_b32_e32 v32, v131
	v_mov_b32_e32 v33, v132
	v_smfmac_f32_16x16x64_f16 v[62:65], v[4:7], a[8:15], v28
	v_smfmac_f32_16x16x64_f16 v[66:69], v[4:7], a[136:143], v28
	global_load_ushort v128, v[114:115], off
	v_smfmac_f32_16x16x64_f16 v[62:65], v[8:11], a[16:23], v28
	v_smfmac_f32_16x16x64_f16 v[66:69], v[8:11], a[144:151], v28
	global_load_ushort v129, v[114:115], off offset:2048
	v_smfmac_f32_16x16x64_f16 v[62:65], v[12:15], a[24:31], v28
	v_smfmac_f32_16x16x64_f16 v[66:69], v[12:15], a[152:159], v28
	global_load_ushort v130, v[116:117], off
	s_waitcnt lgkmcnt(11)
	v_smfmac_f32_16x16x64_f16 v[62:65], v[50:53], a[32:39], v28
	v_smfmac_f32_16x16x64_f16 v[66:69], v[50:53], a[160:167], v28
	global_load_ushort v131, v[116:117], off offset:2048
	s_waitcnt lgkmcnt(10)
	v_smfmac_f32_16x16x64_f16 v[62:65], v[54:57], a[40:47], v28
	v_smfmac_f32_16x16x64_f16 v[66:69], v[54:57], a[168:175], v28
	global_load_ushort v132, v[118:119], off
	s_waitcnt lgkmcnt(9)
	v_smfmac_f32_16x16x64_f16 v[62:65], v[58:61], a[48:55], v28
	v_smfmac_f32_16x16x64_f16 v[66:69], v[58:61], a[176:183], v28
	global_store_dword v[112:113], v46, off
	s_waitcnt lgkmcnt(8)
	v_smfmac_f32_16x16x64_f16 v[62:65], v[70:73], a[56:63], v28
	v_smfmac_f32_16x16x64_f16 v[66:69], v[70:73], a[184:191], v28
	v_cvt_f32_f16_e32 v112, v44
	v_cvt_f32_f16_e32 v113, v43
	v_cvt_f32_f16_e32 v114, v42
	v_cvt_f32_f16_e32 v115, v41
	v_cvt_f32_f16_e32 v118, v45
	v_cndmask_b32_e64 v116, 0, v118, s[22:23]
	v_cndmask_b32_e64 v117, v118, 0, s[22:23]
	s_waitcnt lgkmcnt(7)
	v_smfmac_f32_16x16x64_f16 v[62:65], v[78:81], a[64:71], v28
	v_smfmac_f32_16x16x64_f16 v[66:69], v[78:81], a[192:199], v28
	s_waitcnt lgkmcnt(6)
	v_smfmac_f32_16x16x64_f16 v[62:65], v[82:85], a[72:79], v28
	v_smfmac_f32_16x16x64_f16 v[66:69], v[82:85], a[200:207], v28
	s_waitcnt lgkmcnt(5)
	v_smfmac_f32_16x16x64_f16 v[62:65], v[86:89], a[80:87], v28
	v_smfmac_f32_16x16x64_f16 v[66:69], v[86:89], a[208:215], v28
	s_waitcnt lgkmcnt(4)
	v_smfmac_f32_16x16x64_f16 v[62:65], v[90:93], a[88:95], v28
	v_smfmac_f32_16x16x64_f16 v[66:69], v[90:93], a[216:223], v28
	s_waitcnt lgkmcnt(3)
	v_smfmac_f32_16x16x64_f16 v[62:65], v[94:97], a[96:103], v28
	v_smfmac_f32_16x16x64_f16 v[66:69], v[94:97], a[224:231], v28
	s_waitcnt lgkmcnt(2)
	v_smfmac_f32_16x16x64_f16 v[62:65], v[98:101], a[104:111], v28
	v_smfmac_f32_16x16x64_f16 v[66:69], v[98:101], a[232:239], v28
	s_waitcnt lgkmcnt(1)
	v_smfmac_f32_16x16x64_f16 v[62:65], v[102:105], a[112:119], v28
	v_smfmac_f32_16x16x64_f16 v[66:69], v[102:105], a[240:247], v28
	s_waitcnt lgkmcnt(0)
	v_smfmac_f32_16x16x64_f16 v[62:65], v[106:109], a[120:127], v28
	v_smfmac_f32_16x16x64_f16 v[66:69], v[106:109], a[248:255], v28
	s_nop 6
	v_permlane32_swap_b32_e32 v62, v63
	v_permlane32_swap_b32_e32 v64, v65
	v_permlane32_swap_b32_e32 v66, v67
	v_permlane32_swap_b32_e32 v68, v69
	v_add_f32_e32 v2, v62, v63
	v_add_f32_e32 v0, v64, v65
	v_add_f32_e32 v1, v66, v67
	v_add_f32_e32 v3, v68, v69
